# mLSTM state pass: per-chunk gate values (F, alpha[t], beta[t]) loaded one chunk ahead into spare VGPRs; on top of state-store-move stack
# speedup vs baseline: 1.0020x; 1.0020x over previous
; #define LAS __attribute__((address_space(3)))
; template <int DK, int DVB, bool MLSTM>
; __device__ __forceinline__ void state_unit2(LAS unsigned char* lds, LAS unsigned char* ldstab, const StateArgs a, const int wv) {
;     ...
;     int tid = TIDX(wv); asm volatile("" : "+v"(tid));
;     const int wid = __builtin_amdgcn_readfirstlane(tid >> 6), lane = tid & 63, hi = lane >> 5;
;     const int dkb = wid % NDKB, dvb0 = (wid / NDKB) * BPW;
;     const unsigned ldsb = (unsigned)(uintptr_t)lds;
;     LAS float* wtab = (LAS float*)ldstab;
;     LAS unsigned char* ts = lds + TSOFF + wid * 4096;
;     const unsigned tbA0 = t_base(lane, 0) + (dkb >> 2) * 16384u + 512u * (dkb & 3), tbA1 = t_base(lane, 1) + (dkb >> 2) * 16384u + 512u * (dkb & 3);
;     const unsigned tbB0 = t_base(lane, 0) + VOFF + 512u * dvb0, tbB1 = t_base(lane, 1) + VOFF + 512u * dvb0;
;     f32x16 acc[BPW];
; #pragma unroll
;     for (int j = 0; j < BPW; ++j) acc[j] = (f32x16){};
;     float nacc = 0.f;
;     __syncthreads();
;     ...
;     ST_DMA(0);
; template <int LAYER>
; __device__ __forceinline__ void layer_body(const int lo, const int hi, const bool fused, const int wv) {
;     ...
;                 for (int u0 = F.bid; u0 < 128; u0 += F.G) {
;                     const int u = (F.G == 256) ? ((u0 & 7) * 16 + (u0 >> 3)) : u0;
;                     const int bh = u >> 2, dir = (u >> 1) & 1, dvb = u & 1, b = bh >> 2, h = bh & 3;
;                     la::StateArgs sa; sa.K = (const bf16_t*)(ws + X1_KC) + (size_t)b * SEQ * 512 + h * 128; sa.ldk = 512;
;                     sa.V = (const bf16_t*)(ws + WS_P) + (size_t)b * SEQ * EVEN_INP + PC_VM + h * 128 + dvb * 64; sa.ldv = EVEN_INP;
;                     sa.Cout = (bf16_t*)(ws + X1_CM) + ((size_t)(bh * 2 + dir) * 32) * 128 * 128 + dvb * 64; sa.ldc = 128; sa.cstride = 128 * 128;
;                     sa.Nout = dvb == 0 ? (float*)(ws + X1_NM) + ((size_t)(bh * 2 + dir) * 32) * 128 : nullptr;
;                     sa.alpha = ALPHA + ((size_t)dir * 32 + bh) * SEQ; sa.beta = BETA + ((size_t)dir * 32 + bh) * SEQ; sa.lgam = 0.f; sa.dir = dir;
;                     { const float* mg = BETA + 2 * 32 * SEQ + (dir * 32 + bh) * 8; sa.Mseq = fmaxf(fmaxf(fmaxf(mg[0], mg[1]), fmaxf(mg[2], mg[3])), fmaxf(fmaxf(mg[4], mg[5]), fmaxf(mg[6], mg[7]))); }
;                     la::state_unit2<128, 64, true>(F.lds + LDS_RING, F.lds + LT_X, sa, wv);
.LBB0_553:
	s_lshl_b32 s4, s63, 4
	s_and_b32 s4, s4, 0x70
	s_ashr_i32 s5, s63, 3
	s_add_i32 s6, s4, s5
	s_and_b64 s[4:5], s[10:11], exec
	s_cselect_b32 s4, s6, s63
	s_ashr_i32 s14, s4, 2
	s_bfe_u32 s39, s4, 0x10001
	s_and_b32 s15, s4, 1
	s_ashr_i32 s4, s4, 4
	s_ashr_i32 s5, s4, 31
	s_lshl_b64 s[6:7], s[4:5], 22
	s_add_u32 s5, s45, s6
	s_addc_u32 s6, s46, s7
	s_lshl_b32 s7, s14, 8
	s_and_b32 s7, s7, 0x300
	s_add_u32 s64, s5, s7
	s_addc_u32 s65, s6, 0
	s_mul_hi_i32 s5, s4, 0x1400000
	s_mul_i32 s4, s4, 0x1400000
	s_add_u32 s4, s22, s4
	s_addc_u32 s5, s23, s5
	s_add_u32 s4, s4, s7
	s_addc_u32 s5, s5, 0
	s_lshl_b32 s8, s15, 7
	s_add_u32 s4, s4, s8
	s_addc_u32 s5, s5, 0
	s_add_u32 s36, s4, 0x3a000800
	s_addc_u32 s37, s5, 0
	s_lshl_b32 s4, s14, 1
	s_or_b32 s6, s4, s39
	s_ashr_i32 s7, s6, 31
	s_lshl_b64 s[4:5], s[6:7], 20
	s_add_u32 s4, s48, s4
	s_addc_u32 s5, s49, s5
	s_add_u32 s8, s4, s8
	s_addc_u32 s38, s5, 0
	s_cmp_eq_u32 s15, 0
	s_cselect_b64 s[4:5], -1, 0
	s_lshl_b64 s[6:7], s[6:7], 14
	s_add_u32 s6, s50, s6
	s_addc_u32 s7, s51, s7
	s_lshl_b32 s16, s39, 5
	s_ashr_i32 s15, s14, 31
	s_add_u32 s16, s16, s14
	s_addc_u32 s17, 0, s15
	s_lshl_b64 s[24:25], s[16:17], 14
	s_add_u32 s16, s52, s24
	s_addc_u32 s17, s53, s25
	s_add_u32 s24, s54, s24
	s_addc_u32 s25, s55, s25
	s_lshl_b32 s26, s39, 8
	s_lshl_b32 s27, s14, 3
	s_add_i32 s26, s26, s27
	s_ashr_i32 s27, s26, 31
	s_lshl_b64 s[26:27], s[26:27], 2
	s_add_u32 s26, s56, s26
	s_addc_u32 s27, s57, s27
	global_load_dwordx4 v[0:3], v17, s[26:27]
	global_load_dwordx4 v[4:7], v17, s[26:27] offset:16
	v_mbcnt_lo_u32_b32 v8, -1, 0
	v_mbcnt_hi_u32_b32 v8, -1, v8
	s_mov_b32 s69, 0
	v_or_b32_e32 v18, s19, v8
	s_waitcnt vmcnt(0)
	v_readfirstlane_b32 s26, v18
	s_ashr_i32 s68, s26, 6
	s_ashr_i32 s26, s68, 31
	s_lshr_b32 s26, s26, 30
	s_add_i32 s26, s68, s26
	s_ashr_i32 s71, s26, 2
	s_and_b32 s26, s26, -4
	s_lshl_b32 s27, s68, 12
	s_sub_i32 s72, s68, s26
	s_add_i32 s27, s27, 0
	s_lshl_b32 s26, s72, 9
	s_add_i32 s70, s27, 0x10000
	s_lshl_b32 s73, s71, 9
	s_and_b32 s74, s72, 0xffffc000
	s_and_b32 s75, s26, 0x600
	s_cmp_eq_u32 s39, 0
	s_cselect_b64 s[26:27], -1, 0
	s_and_b64 s[40:41], s[26:27], exec
	v_bfe_u32 v10, v18, 5, 1
	v_bfe_u32 v11, v18, 3, 3
	s_cselect_b32 s39, 0, 0xf80
	v_bfe_u32 v8, v18, 1, 1
	v_and_b32_e32 v15, 2, v11
	v_lshlrev_b32_e32 v16, 1, v10
	s_lshl_b32 s40, s39, 10
	v_and_b32_e32 v9, 12, v18
	v_bitop3_b32 v19, v15, v16, v8 bitop3:0x36
	v_or_b32_e32 v16, 1, v16
	s_add_u32 s40, s64, s40
	v_lshlrev_b32_e32 v12, 3, v18
	v_or_b32_e32 v19, v19, v9
	v_bitop3_b32 v8, v15, v16, v8 bitop3:0x36
	s_addc_u32 s41, s65, 0
	s_bfe_i32 s66, s68, 0x1001d
	v_lshlrev_b32_e32 v14, 11, v10
	v_and_b32_e32 v12, 8, v12
	v_lshl_or_b32 v20, s68, 2, v10
	v_lshlrev_b32_e32 v15, 4, v19
	v_or_b32_e32 v8, v8, v9
	s_lshr_b32 s66, s66, 27
	v_or3_b32 v15, v15, v14, v12
	v_lshl_or_b32 v8, v8, 4, v14
	v_add_u32_e32 v14, s66, v20
	v_or3_b32 v12, v8, v12, s44
	v_and_b32_e32 v8, 0xffffffe0, v14
	v_sub_u32_e32 v16, v20, v8
	v_bfe_u32 v13, v18, 2, 4
	v_lshlrev_b32_e32 v8, 1, v16
	v_bfi_b32 v8, -8, v8, v13
	v_ashrrev_i32_e32 v9, 31, v8
	s_lshl_b32 s67, s68, 1
	s_lshl_b32 s66, s68, 11
	s_add_i32 s76, s66, 0
	s_or_b32 s67, s67, 1
	s_mov_b32 m0, s76
	s_bfe_i32 s77, s67, 0x1001e
	s_barrier
; #define LAS __attribute__((address_space(3)))
; #define TIDX(wv) (((wv) << 6) | lane_id())
; template <int DK, int DVB, bool MLSTM>
; __device__ __forceinline__ void state_unit2(LAS unsigned char* lds, LAS unsigned char* ldstab, const StateArgs a, const int wv) {
;     ...
;     int tid = TIDX(wv); asm volatile("" : "+v"(tid));
;     const int wid = __builtin_amdgcn_readfirstlane(tid >> 6), lane = tid & 63, hi = lane >> 5;
;     const int dkb = wid % NDKB, dvb0 = (wid / NDKB) * BPW;
;     const unsigned ldsb = (unsigned)(uintptr_t)lds;
;     LAS float* wtab = (LAS float*)ldstab;
;     LAS unsigned char* ts = lds + TSOFF + wid * 4096;
;     const unsigned tbA0 = t_base(lane, 0) + (dkb >> 2) * 16384u + 512u * (dkb & 3), tbA1 = t_base(lane, 1) + (dkb >> 2) * 16384u + 512u * (dkb & 3);
;     const unsigned tbB0 = t_base(lane, 0) + VOFF + 512u * dvb0, tbB1 = t_base(lane, 1) + VOFF + 512u * dvb0;
;     f32x16 acc[BPW];
; #pragma unroll
;     for (int j = 0; j < BPW; ++j) acc[j] = (f32x16){};
;     float nacc = 0.f;
;     __syncthreads();
;     ...
;     ST_DMA(0);
;     ...
;             if (MLSTM) { const float F = a.alpha[t0 + (a.dir ? 0 : 127)];
;                 if (tid < 128) wt[tid] = __expf(F - a.alpha[t0 + tid] + a.beta[t0 + tid] - a.Mseq);
	s_lshr_b32 s77, s77, 27
	s_mulk_i32 s39, 0x1400
	v_ashrrev_i32_e32 v19, 31, v18
	v_lshl_add_u64 v[32:33], v[18:19], 2, s[6:7]
	v_lshlrev_b32_e32 v58, 6, v13
	v_lshlrev_b64 v[20:21], 9, v[8:9]
	v_bfe_u32 v51, v18, 3, 4
	v_mov_b32_e32 v44, 1.0
	v_max_f32_e32 v1, v1, v1
	v_max_f32_e32 v0, v0, v0
	v_max_f32_e32 v3, v3, v3
	v_max_f32_e32 v2, v2, v2
	v_max_f32_e32 v7, v7, v7
	v_max_f32_e32 v6, v6, v6
	v_max_f32_e32 v0, v0, v1
	v_max_f32_e32 v1, v2, v3
	v_max_f32_e32 v2, v6, v7
	v_max3_f32 v2, v4, v5, v2
	v_max3_f32 v46, v0, v1, v2
	v_lshrrev_b32_e32 v0, 2, v8
	v_lshlrev_b32_e32 v3, 2, v14
	v_xor_b32_e32 v2, v0, v18
	v_lshlrev_b64 v[0:1], 10, v[8:9]
	v_and_b32_e32 v22, 0xffffff80, v3
	v_lshlrev_b32_e32 v3, 5, v16
	v_lshl_add_u64 v[0:1], s[40:41], 0, v[0:1]
	v_ashrrev_i32_e32 v23, 31, v22
	v_and_b32_e32 v36, 32, v3
	v_lshlrev_b32_e32 v2, 3, v2
	v_lshl_add_u64 v[0:1], v[22:23], 1, v[0:1]
	v_lshlrev_b32_e32 v16, 1, v36
	v_and_b32_e32 v38, 24, v2
	v_lshl_add_u64 v[0:1], v[0:1], 0, v[16:17]
	v_lshlrev_b32_e32 v16, 1, v38
	v_lshl_add_u64 v[0:1], v[0:1], 0, v[16:17]
	global_load_lds_dwordx4 v[0:1], off
	v_lshl_or_b32 v0, s67, 1, v10
	v_add_u32_e32 v2, s77, v0
	v_and_b32_e32 v1, 0xffffffe0, v2
	v_sub_u32_e32 v3, v0, v1
	v_lshlrev_b32_e32 v0, 1, v3
	v_bfi_b32 v0, -8, v0, v13
	v_lshrrev_b32_e32 v1, 2, v0
	v_xor_b32_e32 v4, v1, v18
	v_ashrrev_i32_e32 v1, 31, v0
	v_lshlrev_b32_e32 v2, 2, v2
	v_lshlrev_b64 v[24:25], 9, v[0:1]
	v_lshlrev_b64 v[0:1], 10, v[0:1]
	v_and_b32_e32 v26, 0xffffff80, v2
	v_lshlrev_b32_e32 v2, 5, v3
	s_lshl_b32 s67, s67, 10
	v_lshl_add_u64 v[0:1], s[40:41], 0, v[0:1]
	v_ashrrev_i32_e32 v27, 31, v26
	v_and_b32_e32 v40, 0x60, v2
	v_lshlrev_b32_e32 v2, 3, v4
	s_add_i32 m0, s67, 0
	v_lshl_add_u64 v[0:1], v[26:27], 1, v[0:1]
	v_lshlrev_b32_e32 v16, 1, v40
	v_and_b32_e32 v42, 24, v2
	s_add_u32 s40, s36, s39
	v_lshl_add_u64 v[0:1], v[0:1], 0, v[16:17]
	v_lshlrev_b32_e32 v16, 1, v42
	s_addc_u32 s41, s37, 0
	s_lshl_b32 s39, s68, 3
	v_lshl_add_u64 v[0:1], v[0:1], 0, v[16:17]
	v_and_or_b32 v4, v13, 7, s39
	global_load_lds_dwordx4 v[0:1], off
	v_lshrrev_b32_e32 v0, 2, v4
	v_and_b32_e32 v2, 32, v18
	v_xor_b32_e32 v3, v0, v18
	v_mov_b64_e32 v[0:1], s[40:41]
	v_mad_i64_i32 v[0:1], s[40:41], v4, s60, v[0:1]
	v_lshlrev_b32_e32 v16, 1, v2
	v_lshlrev_b32_e32 v2, 4, v3
	v_lshl_add_u64 v[0:1], v[0:1], 0, v[16:17]
	v_and_b32_e32 v2, 48, v2
	v_mov_b32_e32 v3, v17
	v_lshl_add_u64 v[0:1], v[0:1], 0, v[2:3]
	s_add_i32 m0, s76, 0x4000
	v_mov_b32_e32 v5, v17
	global_load_lds_dwordx4 v[0:1], off
	v_mov_b64_e32 v[0:1], s[36:37]
	v_mad_i64_i32 v[0:1], s[36:37], v4, s60, v[0:1]
	s_lshl_b32 s36, s72, 5
	s_ashr_i32 s37, s36, 31
	s_lshl_b64 s[36:37], s[36:37], 8
	v_lshl_add_u64 v[0:1], v[0:1], 0, v[16:17]
	s_add_u32 s8, s8, s36
	v_lshl_add_u64 v[28:29], v[0:1], 0, v[2:3]
	s_addc_u32 s38, s38, s37
	s_lshl_b32 s36, s71, 5
	v_lshlrev_b32_e32 v0, 1, v18
	s_ashr_i32 s37, s36, 31
	v_and_b32_e32 v1, 62, v0
	s_lshl_b64 s[36:37], s[36:37], 1
	v_add_u32_e32 v35, s70, v1
	v_lshlrev_b32_e32 v1, 6, v11
	s_add_u32 s36, s8, s36
	v_and_b32_e32 v37, 0x100, v1
	v_or_b32_e32 v39, 0xc0, v1
	v_or_b32_e32 v41, 0x2c0, v1
	v_or_b32_e32 v43, 0x4c0, v1
	v_or_b32_e32 v57, 0x6c0, v1
	v_lshlrev_b32_e32 v1, 4, v18
	s_addc_u32 s37, s38, s37
	v_and_b32_e32 v16, 48, v1
	v_lshl_add_u64 v[30:31], s[36:37], 0, v[16:17]
	v_or_b32_e32 v2, 16, v13
	s_and_b64 s[36:37], s[4:5], s[12:13]
	v_cmp_gt_i32_e64 s[4:5], s61, v18
	v_lshlrev_b32_e32 v60, 6, v2
	v_lshlrev_b32_e32 v34, 7, v2
	s_and_b64 s[36:37], s[36:37], s[4:5]
	v_lshrrev_b32_e32 v2, 2, v18
	s_and_b64 s[6:7], s[26:27], exec
	v_and_b32_e32 v50, 8, v2
	v_lshlrev_b32_e32 v2, 7, v18
	v_add_u32_e32 v59, s70, v16
	v_lshlrev_b32_e32 v16, 7, v13
	s_cselect_b32 s68, 0x7f, 0
	s_or_b32 s6, s75, s74
	s_addk_i32 s73, 0x4000
	v_and_b32_e32 v2, 0xffffc000, v2
	v_and_b32_e32 v0, 14, v0
	v_and_b32_e32 v1, 0x600, v1
	v_add_u32_e32 v19, s6, v15
	v_add_u32_e32 v47, s6, v12
	v_add_u32_e32 v48, s73, v15
	v_add_u32_e32 v49, s73, v12
	v_or3_b32 v52, v2, v1, v0
	v_mov_b32_e32 v0, v17
	v_mov_b32_e32 v1, v17
	v_mov_b32_e32 v2, v17
	v_mov_b32_e32 v4, v17
	v_mov_b32_e32 v6, v17
	v_mov_b32_e32 v7, v17
	v_mov_b32_e32 v8, v17
	v_mov_b32_e32 v9, v17
	v_mov_b32_e32 v10, v17
	v_mov_b32_e32 v11, v17
	v_mov_b32_e32 v12, v17
	v_mov_b32_e32 v13, v17
	v_mov_b32_e32 v14, v17
	v_mov_b32_e32 v15, v17
	v_add_u32_e32 v53, v35, v37
	v_add_u32_e32 v54, v35, v39
	v_add_u32_e32 v55, v35, v41
	v_add_u32_e32 v56, v35, v43
	v_add_u32_e32 v57, v35, v57
	v_add_u32_e32 v58, v59, v58
	v_lshlrev_b32_e32 v16, 1, v16
	v_add_u32_e32 v59, v59, v60
	v_lshlrev_b32_e32 v34, 1, v34
	v_lshlrev_b32_e32 v36, 1, v36
	v_lshlrev_b32_e32 v38, 1, v38
	v_lshlrev_b32_e32 v40, 1, v40
	v_lshlrev_b32_e32 v42, 1, v42
	s_mov_b64 s[38:39], 0
	v_mov_b32_e32 v60, v17
	s_mov_b32 s8, 0
	s_sub_i32 s74, 31, s8
	s_and_b64 s[40:41], s[26:27], exec
	s_cselect_b32 s8, s8, s74
	s_lshl_b32 s74, s8, 7
	s_or_b32 s8, s74, s68
	s_lshl_b64 s[40:41], s[8:9], 2
	s_add_u32 s40, s16, s40
	s_addc_u32 s41, s17, s41
	global_load_dword v122, v17, s[40:41]
	s_and_saveexec_b64 s[40:41], s[4:5]
	s_cbranch_execz .Lstpf0p_e
	v_add_u32_e32 v62, s74, v18
	v_ashrrev_i32_e32 v63, 31, v62
	v_lshlrev_b64 v[62:63], 2, v[62:63]
	v_lshl_add_u64 v[64:65], s[16:17], 0, v[62:63]
	v_lshl_add_u64 v[62:63], s[24:25], 0, v[62:63]
	global_load_dword v123, v[64:65], off
	global_load_dword v124, v[62:63], off
.Lstpf0p_e:
	s_or_b64 exec, exec, s[40:41]
	s_branch .LBB0_555

; #define LAS __attribute__((address_space(3)))
; template <int DK, int DVB, bool MLSTM>
; __device__ __forceinline__ void state_unit2(LAS unsigned char* lds, LAS unsigned char* ldstab, const StateArgs a, const int wv) {
;     ...
;         const int ci = hs >> 1, half = hs & 1, c = a.dir ? 31 - ci : ci, t0 = c * 128;
;         LAS float* wt = wtab + (ci & 1) * 128;
;         if (half == 0) {
;             bf16_t* co = a.Cout + (size_t)c * a.cstride + (size_t)(32 * dkb) * a.ldc + 32 * dvb0;
;             if constexpr (BPW == 4) { store_blocks_t<2>(ts, lane, acc, co, a.ldc); store_blocks_t<2>(ts, lane, acc + 2, co + 64, a.ldc); }
;             else store_blocks_t<1>(ts, lane, acc, co, a.ldc);
;             if (MLSTM) { if (a.Nout && tid < DK) a.Nout[(size_t)c * DK + tid] = nacc; }
;             if (MLSTM) { const float F = a.alpha[t0 + (a.dir ? 0 : 127)];
;                 if (tid < 128) wt[tid] = __expf(F - a.alpha[t0 + tid] + a.beta[t0 + tid] - a.Mseq);
;                 eF = __expf(F);
.LBB0_555:
	s_lshl_b32 s6, s69, 8
	s_and_b32 s6, s6, 0x200
	s_add_i32 s73, s6, 0
	s_lshr_b32 s70, s69, 1
	s_and_b32 s72, s69, 1
	s_add_i32 s73, s73, 0x21500
	s_cmp_eq_u32 s72, 0
	s_cselect_b64 s[6:7], -1, 0
	s_cmp_eq_u32 s72, 1
	s_cselect_b64 s[40:41], -1, 0
	s_and_b64 vcc, exec, s[40:41]
	s_cbranch_vccnz .LBB0_561
	s_sub_i32 s8, 31, s70
	s_and_b64 s[40:41], s[26:27], exec
	s_cselect_b32 s8, s70, s8
	s_lshl_b32 s71, s8, 7
	s_or_b32 s8, s71, s68
	s_lshl_b64 s[40:41], s[8:9], 2
	s_add_u32 s40, s16, s40
	s_addc_u32 s41, s17, s41
	s_waitcnt vmcnt(0)
	v_mov_b32_e32 v35, v122
	s_and_saveexec_b64 s[40:41], s[4:5]
	s_cbranch_execz .LBB0_560
	v_add_u32_e32 v62, s71, v18
	v_ashrrev_i32_e32 v63, 31, v62
	v_lshlrev_b64 v[62:63], 2, v[62:63]
	v_lshl_add_u64 v[64:65], s[16:17], 0, v[62:63]
	v_lshl_add_u64 v[62:63], s[24:25], 0, v[62:63]
	v_mov_b32_e32 v37, v123
	v_mov_b32_e32 v39, v124
	s_waitcnt vmcnt(0)
	v_sub_f32_e32 v37, v35, v37
	v_add_f32_e32 v37, v37, v39
	v_sub_f32_e32 v37, v37, v46
	v_mul_f32_e32 v37, 0x3fb8aa3b, v37
	v_exp_f32_e32 v37, v37
	v_lshl_add_u32 v39, v18, 2, s73
	ds_write_b32 v39, v37

; template <int DK, int DVB, bool MLSTM>
; __device__ __forceinline__ void state_unit2(LAS unsigned char* lds, LAS unsigned char* ldstab, const StateArgs a, const int wv) {
;     ...
;             if (MLSTM) { const float F = a.alpha[t0 + (a.dir ? 0 : 127)];
;                 if (tid < 128) wt[tid] = __expf(F - a.alpha[t0 + tid] + a.beta[t0 + tid] - a.Mseq);
.LBB0_563:
	s_andn2_b64 vcc, exec, s[6:7]
	s_cbranch_vccnz .LBB0_565
	s_cmp_lt_u32 s70, 31
	s_cbranch_scc0 .Lstpf0a_skip
	s_add_i32 s8, s70, 1
	s_sub_i32 s74, 31, s8
	s_and_b64 s[40:41], s[26:27], exec
	s_cselect_b32 s8, s8, s74
	s_lshl_b32 s74, s8, 7
	s_or_b32 s8, s74, s68
	s_lshl_b64 s[40:41], s[8:9], 2
	s_add_u32 s40, s16, s40
	s_addc_u32 s41, s17, s41
	global_load_dword v122, v17, s[40:41]
	s_and_saveexec_b64 s[40:41], s[4:5]
	s_cbranch_execz .Lstpf0a_e
	v_add_u32_e32 v62, s74, v18
	v_ashrrev_i32_e32 v63, 31, v62
	v_lshlrev_b64 v[62:63], 2, v[62:63]
	v_lshl_add_u64 v[64:65], s[16:17], 0, v[62:63]
	v_lshl_add_u64 v[62:63], s[24:25], 0, v[62:63]
	global_load_dword v123, v[64:65], off
	global_load_dword v124, v[62:63], off

; #define LAS __attribute__((address_space(3)))
; #define LDS_WAIT() asm volatile("s_waitcnt lgkmcnt(0)" ::: "memory")
; __device__ __forceinline__ bf16_t f2bf(float f) { unsigned u = __builtin_bit_cast(unsigned, f); return (bf16_t)((u + 0x7fffu + ((u >> 16) & 1u)) >> 16); }
; __device__ __forceinline__ int crow(int r, int hi) { return (r & 3) + 8 * (r >> 2) + 4 * hi; }
; __device__ __forceinline__ int crow(int r, int hi) { return (r & 3) + 8 * (r >> 2) + 4 * hi; }
; template <int NBLK>
; __device__ __forceinline__ void store_blocks_t(LAS unsigned char* ts, int lane, const f32x16* blk, bf16_t* dst, int ldd) {
;     constexpr int RB = 64 * NBLK;
;     const int r32 = lane & 31, hi = lane >> 5;
; #pragma unroll
;     for (int j = 0; j < NBLK; ++j)
; #pragma unroll
;         for (int r = 0; r < 16; ++r) *(LAS bf16_t*)(ts + crow(r, hi) * RB + (32 * j + r32) * 2) = f2bf(blk[j][r]);
;     LDS_WAIT();
;     constexpr int CPR = 4 * NBLK, NCH = 32 * CPR;
; #pragma unroll
;     for (int it = 0; it < NCH / 64; ++it) { const int id = it * 64 + lane, row = id / CPR, ch = id % CPR;
;         *(u32x4*)(dst + (size_t)row * ldd + 8 * ch) = *(const LAS u32x4*)(ts + row * RB + ch * 16); }
;     LDS_WAIT();
; template <int DK, int DVB, bool MLSTM>
; __device__ __forceinline__ void state_unit2(LAS unsigned char* lds, LAS unsigned char* ldstab, const StateArgs a, const int wv) {
;     ...
;             bf16_t* co = a.Cout + (size_t)c * a.cstride + (size_t)(32 * dkb) * a.ldc + 32 * dvb0;
;             if constexpr (BPW == 4) { store_blocks_t<2>(ts, lane, acc, co, a.ldc); store_blocks_t<2>(ts, lane, acc + 2, co + 64, a.ldc); }
;             else store_blocks_t<1>(ts, lane, acc, co, a.ldc);
;             if (MLSTM) { if (a.Nout && tid < DK) a.Nout[(size_t)c * DK + tid] = nacc; }
.Lstpf0a_skip:
	v_bfe_u32 v35, v0, 16, 1
	v_add3_u32 v35, v0, v35, s62
	ds_write_b16_d16_hi v53, v35
	v_bfe_u32 v35, v1, 16, 1
	v_add3_u32 v35, v1, v35, s62
	ds_write_b16_d16_hi v53, v35 offset:64
	v_bfe_u32 v35, v2, 16, 1
	v_add3_u32 v35, v2, v35, s62
	ds_write_b16_d16_hi v53, v35 offset:128
	v_bfe_u32 v35, v3, 16, 1
	v_add3_u32 v35, v3, v35, s62
	ds_write_b16_d16_hi v54, v35
	v_bfe_u32 v35, v4, 16, 1
	v_add3_u32 v35, v4, v35, s62
	ds_write_b16_d16_hi v53, v35 offset:512
	v_bfe_u32 v35, v5, 16, 1
	v_add3_u32 v35, v5, v35, s62
	ds_write_b16_d16_hi v53, v35 offset:576
	v_bfe_u32 v35, v6, 16, 1
	v_add3_u32 v35, v6, v35, s62
	ds_write_b16_d16_hi v53, v35 offset:640
	v_bfe_u32 v35, v7, 16, 1
	v_add3_u32 v35, v7, v35, s62
	ds_write_b16_d16_hi v55, v35
	v_bfe_u32 v35, v8, 16, 1
	v_add3_u32 v35, v8, v35, s62
	ds_write_b16_d16_hi v53, v35 offset:1024
	v_bfe_u32 v35, v9, 16, 1
	v_add3_u32 v35, v9, v35, s62
	ds_write_b16_d16_hi v53, v35 offset:1088
	v_bfe_u32 v35, v10, 16, 1
	v_add3_u32 v35, v10, v35, s62
	ds_write_b16_d16_hi v53, v35 offset:1152
	v_bfe_u32 v35, v11, 16, 1
	v_add3_u32 v35, v11, v35, s62
	ds_write_b16_d16_hi v56, v35
	v_bfe_u32 v35, v12, 16, 1
	v_add3_u32 v35, v12, v35, s62
	ds_write_b16_d16_hi v53, v35 offset:1536
	v_bfe_u32 v35, v13, 16, 1
	v_add3_u32 v35, v13, v35, s62
	ds_write_b16_d16_hi v53, v35 offset:1600
	v_bfe_u32 v35, v14, 16, 1
	v_add3_u32 v35, v14, v35, s62
	ds_write_b16_d16_hi v53, v35 offset:1664
	v_bfe_u32 v35, v15, 16, 1
	v_add3_u32 v35, v15, v35, s62
	ds_write_b16_d16_hi v57, v35
	s_sub_i32 s8, 31, s70
	s_waitcnt lgkmcnt(0)
	s_and_b64 s[40:41], s[26:27], exec
	ds_read_b128 v[62:65], v58
	ds_read_b128 v[66:69], v59
	s_cselect_b32 s8, s70, s8
	s_lshl_b64 s[40:41], s[8:9], 15
	v_lshl_add_u64 v[70:71], v[30:31], 0, s[40:41]
	v_lshl_add_u64 v[72:73], v[70:71], 0, v[16:17]
	v_mov_b32_e32 v35, v17
	s_waitcnt lgkmcnt(0)
	global_store_dwordx4 v[72:73], v[62:65], off
	s_nop 1
	v_lshl_add_u64 v[62:63], v[70:71], 0, v[34:35]
	global_store_dwordx4 v[62:63], v[66:69], off
	s_waitcnt lgkmcnt(0)
	s_and_saveexec_b64 s[40:41], s[36:37]
	s_cbranch_execz .Lstmv_558
	s_lshl_b64 s[74:75], s[8:9], 9
	v_lshl_add_u64 v[62:63], v[32:33], 0, s[74:75]
	global_store_dword v[62:63], v60, off

; #define LAS __attribute__((address_space(3)))
; template <int DK, int DVB, bool MLSTM>
; __device__ __forceinline__ void state_unit2(LAS unsigned char* lds, LAS unsigned char* ldstab, const StateArgs a, const int wv) {
;     ...
;     int tid = TIDX(wv); asm volatile("" : "+v"(tid));
;     const int wid = __builtin_amdgcn_readfirstlane(tid >> 6), lane = tid & 63, hi = lane >> 5;
;     const int dkb = wid % NDKB, dvb0 = (wid / NDKB) * BPW;
;     const unsigned ldsb = (unsigned)(uintptr_t)lds;
;     LAS float* wtab = (LAS float*)ldstab;
;     LAS unsigned char* ts = lds + TSOFF + wid * 4096;
;     const unsigned tbA0 = t_base(lane, 0) + (dkb >> 2) * 16384u + 512u * (dkb & 3), tbA1 = t_base(lane, 1) + (dkb >> 2) * 16384u + 512u * (dkb & 3);
;     const unsigned tbB0 = t_base(lane, 0) + VOFF + 512u * dvb0, tbB1 = t_base(lane, 1) + VOFF + 512u * dvb0;
;     f32x16 acc[BPW];
; #pragma unroll
;     for (int j = 0; j < BPW; ++j) acc[j] = (f32x16){};
;     float nacc = 0.f;
;     __syncthreads();
;     ...
;     ST_DMA(0);
; template <int LAYER>
; __device__ __forceinline__ void layer_body(const int lo, const int hi, const bool fused, const int wv) {
;     ...
;                 for (int u0 = F.bid; u0 < 128; u0 += F.G) {
;                     const int u = (F.G == 256) ? ((u0 & 7) * 16 + (u0 >> 3)) : u0;
;                     const int bh = u >> 2, dir = (u >> 1) & 1, dvb = u & 1, b = bh >> 2, h = bh & 3;
;                     la::StateArgs sa; sa.K = (const bf16_t*)(ws + X1_KC) + (size_t)b * SEQ * 512 + h * 128; sa.ldk = 512;
;                     sa.V = (const bf16_t*)(ws + WS_P) + (size_t)b * SEQ * EVEN_INP + PC_VM + h * 128 + dvb * 64; sa.ldv = EVEN_INP;
;                     sa.Cout = (bf16_t*)(ws + X1_CM) + ((size_t)(bh * 2 + dir) * 32) * 128 * 128 + dvb * 64; sa.ldc = 128; sa.cstride = 128 * 128;
;                     sa.Nout = dvb == 0 ? (float*)(ws + X1_NM) + ((size_t)(bh * 2 + dir) * 32) * 128 : nullptr;
;                     sa.alpha = ALPHA + ((size_t)dir * 32 + bh) * SEQ; sa.beta = BETA + ((size_t)dir * 32 + bh) * SEQ; sa.lgam = 0.f; sa.dir = dir;
;                     { const float* mg = BETA + 2 * 32 * SEQ + (dir * 32 + bh) * 8; sa.Mseq = fmaxf(fmaxf(fmaxf(mg[0], mg[1]), fmaxf(mg[2], mg[3])), fmaxf(fmaxf(mg[4], mg[5]), fmaxf(mg[6], mg[7]))); }
;                     la::state_unit2<128, 64, true>(F.lds + LDS_RING, F.lds + LT_X, sa, wv);
.LBB0_3094:
	s_lshl_b32 s4, s63, 4
	s_and_b32 s4, s4, 0x70
	s_ashr_i32 s5, s63, 3
	s_add_i32 s6, s4, s5
	s_and_b64 s[4:5], s[10:11], exec
	s_cselect_b32 s4, s6, s63
	s_ashr_i32 s14, s4, 2
	s_bfe_u32 s39, s4, 0x10001
	s_and_b32 s15, s4, 1
	s_ashr_i32 s4, s4, 4
	s_ashr_i32 s5, s4, 31
	s_lshl_b64 s[6:7], s[4:5], 22
	s_add_u32 s5, s46, s6
	s_addc_u32 s6, s48, s7
	s_lshl_b32 s7, s14, 8
	s_and_b32 s7, s7, 0x300
	s_add_u32 s64, s5, s7
	s_addc_u32 s65, s6, 0
	s_mul_hi_i32 s5, s4, 0x1400000
	s_mul_i32 s4, s4, 0x1400000
	s_add_u32 s4, s22, s4
	s_addc_u32 s5, s23, s5
	s_add_u32 s4, s4, s7
	s_addc_u32 s5, s5, 0
	s_lshl_b32 s8, s15, 7
	s_add_u32 s4, s4, s8
	s_addc_u32 s5, s5, 0
	s_add_u32 s36, s4, 0x3a000800
	s_addc_u32 s37, s5, 0
	s_lshl_b32 s4, s14, 1
	s_or_b32 s6, s4, s39
	s_ashr_i32 s7, s6, 31
	s_lshl_b64 s[4:5], s[6:7], 20
	s_add_u32 s4, s49, s4
	s_addc_u32 s5, s50, s5
	s_add_u32 s8, s4, s8
	s_addc_u32 s38, s5, 0
	s_cmp_eq_u32 s15, 0
	s_cselect_b64 s[4:5], -1, 0
	s_lshl_b64 s[6:7], s[6:7], 14
	s_add_u32 s6, s51, s6
	s_addc_u32 s7, s55, s7
	s_lshl_b32 s16, s39, 5
	s_ashr_i32 s15, s14, 31
	s_add_u32 s16, s16, s14
	s_addc_u32 s17, 0, s15
	s_lshl_b64 s[24:25], s[16:17], 14
	s_add_u32 s16, s47, s24
	s_addc_u32 s17, s52, s25
	s_add_u32 s24, s53, s24
	s_addc_u32 s25, s54, s25
	s_lshl_b32 s26, s39, 8
	s_lshl_b32 s27, s14, 3
	s_add_i32 s26, s26, s27
	s_ashr_i32 s27, s26, 31
	s_lshl_b64 s[26:27], s[26:27], 2
	s_add_u32 s26, s56, s26
	s_addc_u32 s27, s57, s27
	global_load_dwordx4 v[0:3], v17, s[26:27]
	global_load_dwordx4 v[4:7], v17, s[26:27] offset:16
	v_mbcnt_lo_u32_b32 v8, -1, 0
	v_mbcnt_hi_u32_b32 v8, -1, v8
	s_mov_b32 s69, 0
	v_or_b32_e32 v18, s19, v8
	s_nop 0
	v_readfirstlane_b32 s26, v18
	s_ashr_i32 s68, s26, 6
	s_ashr_i32 s26, s68, 31
	s_lshr_b32 s26, s26, 30
	s_add_i32 s26, s68, s26
	s_ashr_i32 s71, s26, 2
	s_and_b32 s26, s26, -4
	s_lshl_b32 s27, s68, 12
	s_sub_i32 s72, s68, s26
	s_add_i32 s27, s27, 0
	s_lshl_b32 s26, s72, 9
	s_add_i32 s70, s27, 0x10000
	s_lshl_b32 s73, s71, 9
	s_and_b32 s74, s72, 0xffffc000
	s_and_b32 s75, s26, 0x600
	s_cmp_eq_u32 s39, 0
	s_cselect_b64 s[26:27], -1, 0
	s_and_b64 s[40:41], s[26:27], exec
	v_bfe_u32 v10, v18, 5, 1
	v_bfe_u32 v11, v18, 3, 3
	s_cselect_b32 s39, 0, 0xf80
	v_bfe_u32 v8, v18, 1, 1
	v_and_b32_e32 v15, 2, v11
	v_lshlrev_b32_e32 v16, 1, v10
	s_lshl_b32 s40, s39, 10
	v_and_b32_e32 v9, 12, v18
	v_bitop3_b32 v19, v15, v16, v8 bitop3:0x36
	v_or_b32_e32 v16, 1, v16
	s_add_u32 s40, s64, s40
	v_lshlrev_b32_e32 v12, 3, v18
	v_or_b32_e32 v19, v19, v9
	v_bitop3_b32 v8, v15, v16, v8 bitop3:0x36
	s_addc_u32 s41, s65, 0
	s_bfe_i32 s66, s68, 0x1001d
	v_lshlrev_b32_e32 v14, 11, v10
	v_and_b32_e32 v12, 8, v12
	v_lshl_or_b32 v20, s68, 2, v10
	v_lshlrev_b32_e32 v15, 4, v19
	v_or_b32_e32 v8, v8, v9
	s_lshr_b32 s66, s66, 27
	v_or3_b32 v15, v15, v14, v12
	v_lshl_or_b32 v8, v8, 4, v14
	v_add_u32_e32 v14, s66, v20
	v_or3_b32 v12, v8, v12, s44
	v_and_b32_e32 v8, 0xffffffe0, v14
	v_sub_u32_e32 v16, v20, v8
	v_bfe_u32 v13, v18, 2, 4
	v_lshlrev_b32_e32 v8, 1, v16
	v_bfi_b32 v8, -8, v8, v13
	v_ashrrev_i32_e32 v9, 31, v8
	s_lshl_b32 s67, s68, 1
	s_lshl_b32 s66, s68, 11
	s_add_i32 s76, s66, 0
	s_or_b32 s67, s67, 1
	s_mov_b32 m0, s76
	s_bfe_i32 s77, s67, 0x1001e
	s_barrier
; #define LAS __attribute__((address_space(3)))
; #define TIDX(wv) (((wv) << 6) | lane_id())
; template <int DK, int DVB, bool MLSTM>
; __device__ __forceinline__ void state_unit2(LAS unsigned char* lds, LAS unsigned char* ldstab, const StateArgs a, const int wv) {
;     ...
;     int tid = TIDX(wv); asm volatile("" : "+v"(tid));
;     const int wid = __builtin_amdgcn_readfirstlane(tid >> 6), lane = tid & 63, hi = lane >> 5;
;     const int dkb = wid % NDKB, dvb0 = (wid / NDKB) * BPW;
;     const unsigned ldsb = (unsigned)(uintptr_t)lds;
;     LAS float* wtab = (LAS float*)ldstab;
;     LAS unsigned char* ts = lds + TSOFF + wid * 4096;
;     const unsigned tbA0 = t_base(lane, 0) + (dkb >> 2) * 16384u + 512u * (dkb & 3), tbA1 = t_base(lane, 1) + (dkb >> 2) * 16384u + 512u * (dkb & 3);
;     const unsigned tbB0 = t_base(lane, 0) + VOFF + 512u * dvb0, tbB1 = t_base(lane, 1) + VOFF + 512u * dvb0;
;     f32x16 acc[BPW];
; #pragma unroll
;     for (int j = 0; j < BPW; ++j) acc[j] = (f32x16){};
;     float nacc = 0.f;
;     __syncthreads();
;     ...
;     ST_DMA(0);
;     ...
;             if (MLSTM) { const float F = a.alpha[t0 + (a.dir ? 0 : 127)];
;                 if (tid < 128) wt[tid] = __expf(F - a.alpha[t0 + tid] + a.beta[t0 + tid] - a.Mseq);
	s_lshr_b32 s77, s77, 27
	s_mulk_i32 s39, 0x1400
	v_ashrrev_i32_e32 v19, 31, v18
	v_lshl_add_u64 v[32:33], v[18:19], 2, s[6:7]
	v_lshlrev_b32_e32 v58, 6, v13
	v_lshlrev_b64 v[20:21], 9, v[8:9]
	v_bfe_u32 v51, v18, 3, 4
	v_mov_b32_e32 v44, 1.0
	s_waitcnt vmcnt(1)
	v_max_f32_e32 v1, v1, v1
	v_max_f32_e32 v0, v0, v0
	v_max_f32_e32 v3, v3, v3
	v_max_f32_e32 v2, v2, v2
	s_waitcnt vmcnt(0)
	v_max_f32_e32 v7, v7, v7
	v_max_f32_e32 v6, v6, v6
	v_max_f32_e32 v0, v0, v1
	v_max_f32_e32 v1, v2, v3
	v_max_f32_e32 v2, v6, v7
	v_max3_f32 v2, v4, v5, v2
	v_max3_f32 v46, v0, v1, v2
	v_lshrrev_b32_e32 v0, 2, v8
	v_lshlrev_b32_e32 v3, 2, v14
	v_xor_b32_e32 v2, v0, v18
	v_lshlrev_b64 v[0:1], 10, v[8:9]
	v_and_b32_e32 v22, 0xffffff80, v3
	v_lshlrev_b32_e32 v3, 5, v16
	v_lshl_add_u64 v[0:1], s[40:41], 0, v[0:1]
	v_ashrrev_i32_e32 v23, 31, v22
	v_and_b32_e32 v36, 32, v3
	v_lshlrev_b32_e32 v2, 3, v2
	v_lshl_add_u64 v[0:1], v[22:23], 1, v[0:1]
	v_lshlrev_b32_e32 v16, 1, v36
	v_and_b32_e32 v38, 24, v2
	v_lshl_add_u64 v[0:1], v[0:1], 0, v[16:17]
	v_lshlrev_b32_e32 v16, 1, v38
	v_lshl_add_u64 v[0:1], v[0:1], 0, v[16:17]
	global_load_lds_dwordx4 v[0:1], off
	v_lshl_or_b32 v0, s67, 1, v10
	v_add_u32_e32 v2, s77, v0
	v_and_b32_e32 v1, 0xffffffe0, v2
	v_sub_u32_e32 v3, v0, v1
	v_lshlrev_b32_e32 v0, 1, v3
	v_bfi_b32 v0, -8, v0, v13
	v_lshrrev_b32_e32 v1, 2, v0
	v_xor_b32_e32 v4, v1, v18
	v_ashrrev_i32_e32 v1, 31, v0
	v_lshlrev_b32_e32 v2, 2, v2
	v_lshlrev_b64 v[24:25], 9, v[0:1]
	v_lshlrev_b64 v[0:1], 10, v[0:1]
	v_and_b32_e32 v26, 0xffffff80, v2
	v_lshlrev_b32_e32 v2, 5, v3
	s_lshl_b32 s67, s67, 10
	v_lshl_add_u64 v[0:1], s[40:41], 0, v[0:1]
	v_ashrrev_i32_e32 v27, 31, v26
	v_and_b32_e32 v40, 0x60, v2
	v_lshlrev_b32_e32 v2, 3, v4
	s_add_i32 m0, s67, 0
	v_lshl_add_u64 v[0:1], v[26:27], 1, v[0:1]
	v_lshlrev_b32_e32 v16, 1, v40
	v_and_b32_e32 v42, 24, v2
	s_add_u32 s40, s36, s39
	v_lshl_add_u64 v[0:1], v[0:1], 0, v[16:17]
	v_lshlrev_b32_e32 v16, 1, v42
	s_addc_u32 s41, s37, 0
	s_lshl_b32 s39, s68, 3
	v_lshl_add_u64 v[0:1], v[0:1], 0, v[16:17]
	v_and_or_b32 v4, v13, 7, s39
	global_load_lds_dwordx4 v[0:1], off
	v_lshrrev_b32_e32 v0, 2, v4
	v_and_b32_e32 v2, 32, v18
	v_xor_b32_e32 v3, v0, v18
	v_mov_b64_e32 v[0:1], s[40:41]
	v_mad_i64_i32 v[0:1], s[40:41], v4, s60, v[0:1]
	v_lshlrev_b32_e32 v16, 1, v2
	v_lshlrev_b32_e32 v2, 4, v3
	v_lshl_add_u64 v[0:1], v[0:1], 0, v[16:17]
	v_and_b32_e32 v2, 48, v2
	v_mov_b32_e32 v3, v17
	v_lshl_add_u64 v[0:1], v[0:1], 0, v[2:3]
	s_add_i32 m0, s76, 0x4000
	v_mov_b32_e32 v5, v17
	global_load_lds_dwordx4 v[0:1], off
	v_mov_b64_e32 v[0:1], s[36:37]
	v_mad_i64_i32 v[0:1], s[36:37], v4, s60, v[0:1]
	s_lshl_b32 s36, s72, 5
	s_ashr_i32 s37, s36, 31
	s_lshl_b64 s[36:37], s[36:37], 8
	v_lshl_add_u64 v[0:1], v[0:1], 0, v[16:17]
	s_add_u32 s8, s8, s36
	v_lshl_add_u64 v[28:29], v[0:1], 0, v[2:3]
	s_addc_u32 s38, s38, s37
	s_lshl_b32 s36, s71, 5
	v_lshlrev_b32_e32 v0, 1, v18
	s_ashr_i32 s37, s36, 31
	v_and_b32_e32 v1, 62, v0
	s_lshl_b64 s[36:37], s[36:37], 1
	v_add_u32_e32 v35, s70, v1
	v_lshlrev_b32_e32 v1, 6, v11
	s_add_u32 s36, s8, s36
	v_and_b32_e32 v37, 0x100, v1
	v_or_b32_e32 v39, 0xc0, v1
	v_or_b32_e32 v41, 0x2c0, v1
	v_or_b32_e32 v43, 0x4c0, v1
	v_or_b32_e32 v57, 0x6c0, v1
	v_lshlrev_b32_e32 v1, 4, v18
	s_addc_u32 s37, s38, s37
	v_and_b32_e32 v16, 48, v1
	v_lshl_add_u64 v[30:31], s[36:37], 0, v[16:17]
	v_or_b32_e32 v2, 16, v13
	s_and_b64 s[36:37], s[4:5], s[12:13]
	v_cmp_gt_i32_e64 s[4:5], s61, v18
	v_lshlrev_b32_e32 v60, 6, v2
	v_lshlrev_b32_e32 v34, 7, v2
	s_and_b64 s[36:37], s[36:37], s[4:5]
	v_lshrrev_b32_e32 v2, 2, v18
	s_and_b64 s[6:7], s[26:27], exec
	v_and_b32_e32 v50, 8, v2
	v_lshlrev_b32_e32 v2, 7, v18
	v_add_u32_e32 v59, s70, v16
	v_lshlrev_b32_e32 v16, 7, v13
	s_cselect_b32 s68, 0x7f, 0
	s_or_b32 s6, s75, s74
	s_addk_i32 s73, 0x4000
	v_and_b32_e32 v2, 0xffffc000, v2
	v_and_b32_e32 v0, 14, v0
	v_and_b32_e32 v1, 0x600, v1
	v_add_u32_e32 v19, s6, v15
	v_add_u32_e32 v47, s6, v12
	v_add_u32_e32 v48, s73, v15
	v_add_u32_e32 v49, s73, v12
	v_or3_b32 v52, v2, v1, v0
	v_mov_b32_e32 v0, v17
	v_mov_b32_e32 v1, v17
	v_mov_b32_e32 v2, v17
	v_mov_b32_e32 v4, v17
	v_mov_b32_e32 v6, v17
	v_mov_b32_e32 v7, v17
	v_mov_b32_e32 v8, v17
	v_mov_b32_e32 v9, v17
	v_mov_b32_e32 v10, v17
	v_mov_b32_e32 v11, v17
	v_mov_b32_e32 v12, v17
	v_mov_b32_e32 v13, v17
	v_mov_b32_e32 v14, v17
	v_mov_b32_e32 v15, v17
	v_add_u32_e32 v53, v35, v37
	v_add_u32_e32 v54, v35, v39
	v_add_u32_e32 v55, v35, v41
	v_add_u32_e32 v56, v35, v43
	v_add_u32_e32 v57, v35, v57
	v_add_u32_e32 v58, v59, v58
	v_lshlrev_b32_e32 v16, 1, v16
	v_add_u32_e32 v59, v59, v60
	v_lshlrev_b32_e32 v34, 1, v34
	v_lshlrev_b32_e32 v36, 1, v36
	v_lshlrev_b32_e32 v38, 1, v38
	v_lshlrev_b32_e32 v40, 1, v40
	v_lshlrev_b32_e32 v42, 1, v42
	s_mov_b64 s[38:39], 0
	v_mov_b32_e32 v60, v17
	s_mov_b32 s8, 0
	s_sub_i32 s74, 31, s8
	s_and_b64 s[40:41], s[26:27], exec
	s_cselect_b32 s8, s8, s74
	s_lshl_b32 s74, s8, 7
	s_or_b32 s8, s74, s68
	s_lshl_b64 s[40:41], s[8:9], 2
	s_add_u32 s40, s16, s40
	s_addc_u32 s41, s17, s41
	global_load_dword v122, v17, s[40:41]
	s_and_saveexec_b64 s[40:41], s[4:5]
	s_cbranch_execz .Lstpf1p_e
	v_add_u32_e32 v62, s74, v18
	v_ashrrev_i32_e32 v63, 31, v62
	v_lshlrev_b64 v[62:63], 2, v[62:63]
	v_lshl_add_u64 v[64:65], s[16:17], 0, v[62:63]
	v_lshl_add_u64 v[62:63], s[24:25], 0, v[62:63]
	global_load_dword v123, v[64:65], off
	global_load_dword v124, v[62:63], off
